# speedup vs baseline: 1.0014x; 1.0014x over previous
.LBB0_89:
	s_or_b64 exec, exec, s[8:9]
	v_mov_b32_e32 v3, 0
	v_lshlrev_b32_e32 v70, 4, v28
	s_and_saveexec_b64 s[60:61], vcc
	s_cbranch_execz .LBB0_118
	s_mov_b64 s[92:93], s[14:15]
	v_lshl_add_u64 v[22:23], s[12:13], 0, v[2:3]
	s_waitcnt vmcnt(0)
	v_cndmask_b32_e64 v55, -1, v4, s[0:1]
	s_movk_i32 s0, 0x880
	v_mov_b32_e32 v2, 0x1dd00
	v_mad_u32_u24 v4, v80, s0, v2
	v_lshlrev_b32_e32 v2, 1, v1
	v_mov_b32_e32 v27, v3
	v_mbcnt_hi_u32_b32 v2, -1, v29
	v_lshl_add_u64 v[72:73], v[22:23], 0, v[26:27]
	v_and_b32_e32 v23, 64, v2
	v_xor_b32_e32 v22, 16, v2
	v_add_u32_e32 v23, 64, v23
	v_cmp_lt_i32_e32 vcc, v22, v23
	v_lshlrev_b32_e32 v88, 2, v28
	v_and_b32_e32 v24, 7, v0
	v_cndmask_b32_e32 v22, v2, v22, vcc
	v_lshlrev_b32_e32 v90, 2, v22
	v_xor_b32_e32 v22, 32, v2
	v_cmp_lt_i32_e32 vcc, v22, v23
	s_mov_b32 s24, 0x10000
	v_cndmask_b32_e32 v2, v2, v22, vcc
	v_lshlrev_b32_e32 v91, 2, v2
	v_lshrrev_b32_e32 v2, 2, v79
	v_mul_u32_u24_e32 v22, 0x88, v79
	v_add3_u32 v92, v4, v22, v1
	v_or_b32_e32 v2, v88, v2
	v_lshlrev_b32_e32 v22, 3, v0
	v_mul_u32_u24_e32 v2, 0x88, v2
	v_and_b32_e32 v22, 24, v22
	v_add3_u32 v93, v4, v2, v22
	v_lshlrev_b32_e32 v2, 5, v24
	v_or3_b32 v78, v2, v1, s24
	v_bfe_u32 v2, v0, 1, 2
	v_lshrrev_b32_e32 v89, 3, v79
	v_lshl_or_b32 v88, v89, 4, v88
	v_cmp_eq_u32_e64 s[6:7], 4, v24
	v_cmp_eq_u32_e64 s[8:9], 3, v24
	v_cmp_eq_u32_e64 s[10:11], 2, v24
	v_cmp_eq_u32_e64 s[12:13], 1, v24
	v_cmp_eq_u32_e64 s[14:15], 0, v24
	v_cmp_eq_u32_e64 s[16:17], 7, v24
	v_cmp_eq_u32_e64 s[18:19], 6, v24
	v_cmp_eq_u32_e64 s[20:21], 5, v24
	v_cmp_eq_u32_e64 s[22:23], 0, v2
	v_cmp_eq_u32_e64 s[24:25], 1, v2
	v_cmp_eq_u32_e64 s[26:27], 2, v2
	v_cmp_eq_u32_e64 s[28:29], 3, v2
	s_and_b64 s[22:23], s[22:23], s[4:5]
	s_and_b64 s[24:25], s[24:25], s[4:5]
	s_and_b64 s[26:27], s[26:27], s[4:5]
	s_and_b64 s[28:29], s[28:29], s[4:5]
	v_mov_b32_e32 v71, 0xf149f2ca
	s_mov_b64 s[62:63], 0
	s_mov_b32 s69, 0xf149f2ca
	s_mov_b32 s70, 0xefa18f08
	s_mov_b32 s71, 0x41000000
	s_movk_i32 s72, 0x110
	s_mov_b32 s77, 0x26500
	s_mov_b32 s73, 0x2650c
	s_mov_b32 s80, -1
	s_mov_b32 s81, 0
	s_mov_b32 s82, 0
	s_mov_b32 s83, 0x7fffffff
	s_mov_b64 s[84:85], 0
	v_mov_b32_e32 v100, 0
	v_mov_b32_e32 v4, 0
	v_mov_b32_e32 v103, 0xf149f2ca
	v_mov_b32_e32 v46, v3
	v_mov_b32_e32 v47, v3
	v_mov_b32_e32 v48, v3
	v_mov_b32_e32 v49, v3
	v_mov_b32_e32 v50, v3
	v_mov_b32_e32 v51, v3
	v_mov_b32_e32 v52, v3
	v_mov_b32_e32 v53, v3
	v_mov_b32_e32 v38, v3
	v_mov_b32_e32 v39, v3
	v_mov_b32_e32 v40, v3
	v_mov_b32_e32 v41, v3
	v_mov_b32_e32 v42, v3
	v_mov_b32_e32 v43, v3
	v_mov_b32_e32 v44, v3
	v_mov_b32_e32 v45, v3
	v_mov_b32_e32 v30, v3
	v_mov_b32_e32 v31, v3
	v_mov_b32_e32 v32, v3
	v_mov_b32_e32 v33, v3
	v_mov_b32_e32 v34, v3
	v_mov_b32_e32 v35, v3
	v_mov_b32_e32 v36, v3
	v_mov_b32_e32 v37, v3
	v_mov_b32_e32 v22, v3
	v_mov_b32_e32 v23, v3
	v_mov_b32_e32 v24, v3
	v_mov_b32_e32 v25, v3
	v_mov_b32_e32 v26, v3
	v_mov_b32_e32 v28, v3
	v_mov_b32_e32 v29, v3
	v_readfirstlane_b32 s86, v80
	s_mov_b32 s87, 0
	v_readfirstlane_b32 s88, v99
	v_readfirstlane_b32 s89, v5
	v_readfirstlane_b32 s96, v54
	v_readfirstlane_b32 s97, v84
	v_readfirstlane_b32 s98, v85
	v_readfirstlane_b32 s99, v81
	v_readfirstlane_b32 s100, v83
	v_readfirstlane_b32 s101, v82
	s_cmp_ge_i32 s96, s68
	s_cselect_b32 s100, 0, s100
	s_branch .LBB0_95

.LBB0_97:
	s_or_b64 exec, exec, s[40:41]
	global_load_dword v98, v108, s[58:59]
	global_load_dwordx4 v[74:77], v2, s[92:93]
	global_load_dwordx4 v[94:97], v2, s[92:93] offset:64
	global_load_dwordx4 v[120:123], v2, s[92:93] offset:128
	global_load_dwordx4 v[124:127], v2, s[92:93] offset:192
	s_cmp_lt_i32 s80, 0
	s_cbranch_scc1 .Lattn_skip
	v_mfma_f32_16x16x32_f16 v[104:107], v[66:69], v[6:9], 0
	s_and_b32 s95, s84, 0xffff
	s_sub_i32 s42, s82, s94
	s_max_i32 s42, s42, 0
	s_min_i32 s42, s42, 16
	s_lshl_b32 s43, 1, s42
	s_add_i32 s43, s43, -1
	v_mfma_f32_16x16x32_f16 v[104:107], v[62:65], v[10:13], v[104:107]
	s_and_b32 s42, s95, s43
	s_andn2_b32 s43, s95, s43
	s_lshl_b32 s43, s43, 16
	s_or_b32 s95, s42, s43
	v_mfma_f32_16x16x32_f16 v[104:107], v[58:61], v[14:17], v[104:107]
	v_cmp_ngt_f32_e64 s[48:49], s70, v103
	v_mfma_f32_16x16x32_f16 v[108:111], v[54:57], v[18:21], v[104:107]
	v_lshrrev_b32_e64 v2, v88, s95
	s_nop 1
	v_and_b32_e32 v5, 1, v2
	v_cmp_eq_u32_e64 s[46:47], 0, v5
	v_and_b32_e32 v5, 2, v2
	v_cmp_eq_u32_e64 s[40:41], 0, v5
	v_and_b32_e32 v104, 4, v2
	v_and_b32_e32 v2, 8, v2
	s_nop 0
	v_cndmask_b32_e64 v107, v108, v71, s[46:47]
	v_cndmask_b32_e64 v105, v109, v71, s[40:41]
	v_cmp_eq_u32_e64 s[42:43], 0, v104
	v_cmp_eq_u32_e64 s[44:45], 0, v2
	v_max3_f32 v5, v107, s69, v105
	v_cndmask_b32_e64 v106, v110, v71, s[42:43]
	v_cndmask_b32_e64 v104, v111, v71, s[44:45]
	v_max3_f32 v2, v5, v106, v104
	v_mov_b32_e32 v5, v2
	s_nop 1
	v_permlane16_swap_b32_e32 v5, v2
	v_max_f32_e32 v2, v2, v5
	v_mov_b32_e32 v5, v2
	s_nop 1
	v_permlane32_swap_b32_e32 v5, v2
	v_max_f32_e32 v108, v2, v5
	v_sub_f32_e32 v2, v108, v103
	v_cmp_lt_f32_e32 vcc, s71, v2
	s_and_b64 vcc, s[48:49], vcc
	s_nop 0
	v_cndmask_b32_e64 v2, 0, 1, vcc
	v_cmp_ne_u32_e64 s[50:51], 0, v2
	s_cmp_lg_u64 s[50:51], 0
	s_cselect_b64 s[50:51], -1, 0
	s_cbranch_vccz .LBB0_117
	v_max_f32_e32 v2, v108, v108
	v_max_f32_e32 v5, v103, v103
	v_max_f32_e32 v5, v5, v2
	v_sub_f32_e32 v2, v103, v5
	v_exp_f32_e32 v2, v2
	s_cbranch_execnz .LBB0_100
